# att5_hoist_first_V_fragment_block
# baseline (speedup 1.0000x reference)
; __device__ __forceinline__ void qkt64c(f32x16& p0, f32x16& p1, const char* Ks, const bf16x8* qr, const f32x16& cinit, int r32, int hi) {
; #pragma unroll
;     for (int d0 = 0; d0 < 4; ++d0) { const int cb = (d0 * 16 + hi * 8) * 2;
;         const bf16x8 b0 = *reinterpret_cast<const bf16x8*>(Ks + kswz<64>(r32, cb));
;         const bf16x8 b1 = *reinterpret_cast<const bf16x8*>(Ks + kswz<64>(32 + r32, cb));
;         if (d0 == 0) { p0 = __builtin_amdgcn_mfma_f32_32x32x16_bf16(b0, qr[0], cinit, 0, 0, 0); p1 = __builtin_amdgcn_mfma_f32_32x32x16_bf16(b1, qr[0], cinit, 0, 0, 0); }
;         else { p0 = __builtin_amdgcn_mfma_f32_32x32x16_bf16(b0, qr[d0], p0, 0, 0, 0); p1 = __builtin_amdgcn_mfma_f32_32x32x16_bf16(b1, qr[d0], p1, 0, 0, 0); } }
; }
.LBB0_823:
	s_lshl_b32 s2, s42, 13
	s_add_i32 s2, s2, 0
	v_add_u32_e32 v128, s2, v223
	ds_read_b128 v[144:147], v128 offset:49152
	v_add_u32_e32 v129, s2, v226
	ds_read_b128 v[148:151], v129 offset:49152
	v_add_u32_e32 v130, s2, v228
	ds_read_b128 v[152:155], v130 offset:49152
	v_add_u32_e32 v131, s2, v229
	ds_read_b128 v[156:159], v131 offset:49152
	ds_read_b128 v[232:235], v128 offset:53248
	ds_read_b128 v[236:239], v129 offset:53248
	ds_read_b128 v[240:243], v130 offset:53248
	ds_read_b128 v[244:247], v131 offset:53248
	v_lshl_add_u64 v[202:203], v[200:201], 0, s[64:65]
	s_mov_b32 s2, 0x8a40000
	v_add_co_u32_e32 v64, vcc, s2, v202
	s_mov_b32 s2, 0x8a50000
	s_nop 0
	v_addc_co_u32_e32 v65, vcc, 0, v203, vcc
	v_add_co_u32_e32 v66, vcc, s2, v202
	v_lshl_add_u64 v[204:205], v[198:199], 0, s[64:65]
	s_nop 0
	v_addc_co_u32_e32 v67, vcc, 0, v203, vcc
	s_mov_b32 s2, 0x6a40000
	global_load_dwordx4 v[178:181], v[64:65], off
	global_load_dwordx4 v[182:185], v[66:67], off
	v_add_co_u32_e32 v64, vcc, s2, v204
	s_nop 1
	v_addc_co_u32_e32 v65, vcc, 0, v205, vcc
	global_load_dwordx4 v[186:189], v[64:65], off
	v_exp_f32_e32 v190, v120
	v_exp_f32_e32 v191, v121
	v_add_f32_e32 v120, v96, v97
	v_add_f32_e32 v121, v98, v99
	s_waitcnt lgkmcnt(7)
	v_mfma_f32_32x32x16_bf16 v[128:143], v[144:147], v[162:165], v[80:95]
	v_exp_f32_e32 v192, v122
	v_add_f32_e32 v120, v120, v121
	v_add_f32_e32 v121, v100, v101
	v_add_f32_e32 v122, v102, v103
	v_exp_f32_e32 v193, v123
	s_waitcnt lgkmcnt(6)
	v_mfma_f32_32x32x16_bf16 v[128:143], v[148:151], v[166:169], v[128:143]
	v_add_f32_e32 v121, v121, v122
	v_add_f32_e32 v122, v104, v105
	v_add_f32_e32 v123, v106, v107
	v_add_f32_e32 v122, v122, v123
	v_add_f32_e32 v123, v108, v109
	s_waitcnt lgkmcnt(5)
	v_mfma_f32_32x32x16_bf16 v[128:143], v[152:155], v[170:173], v[128:143]
	v_add_f32_e32 v208, v110, v111
	v_add_f32_e32 v123, v123, v208
	v_add_f32_e32 v208, v112, v113
	v_add_f32_e32 v209, v114, v115
	v_add_f32_e32 v208, v208, v209
	s_waitcnt lgkmcnt(4)
	v_mfma_f32_32x32x16_bf16 v[128:143], v[156:159], v[174:177], v[128:143]
	v_exp_f32_e32 v124, v124
	v_exp_f32_e32 v125, v125
	s_waitcnt lgkmcnt(3)
	v_mfma_f32_32x32x16_bf16 v[144:159], v[232:235], v[162:165], v[80:95]
	v_lshl_add_u32 v234, s12, 14, v217
	ds_read_b64_tr_b16 v[64:65], v234 offset:0
	ds_read_b64_tr_b16 v[66:67], v234 offset:0x800
	ds_read_b64_tr_b16 v[68:69], v234 offset:0x1000
	ds_read_b64_tr_b16 v[70:71], v234 offset:0x1800
	ds_read_b64_tr_b16 v[72:73], v234 offset:0x2000
	ds_read_b64_tr_b16 v[74:75], v234 offset:0x2800
	ds_read_b64_tr_b16 v[76:77], v234 offset:0x3000
	ds_read_b64_tr_b16 v[78:79], v234 offset:0x3800
	v_exp_f32_e32 v126, v126
	v_exp_f32_e32 v127, v127
	v_add_f32_e32 v120, v208, v120
	v_add_f32_e32 v208, v116, v117
	v_add_f32_e32 v209, v118, v119
	v_add_f32_e32 v208, v208, v209
	v_add_f32_e32 v121, v208, v121
	s_waitcnt lgkmcnt(10)
	v_mfma_f32_32x32x16_bf16 v[144:159], v[236:239], v[166:169], v[144:159]
	v_add_f32_e32 v208, v190, v191
	v_add_f32_e32 v209, v192, v193
	v_add_f32_e32 v208, v208, v209
	v_add_f32_e32 v122, v122, v208
	v_add_f32_e32 v208, v124, v125
	v_add_f32_e32 v209, v126, v127
	v_add_f32_e32 v208, v208, v209
	s_waitcnt lgkmcnt(9)
	v_mfma_f32_32x32x16_bf16 v[144:159], v[240:243], v[170:173], v[144:159]
	v_add_f32_e32 v123, v123, v208
	v_add_f32_e32 v120, v120, v121
	v_add_f32_e32 v121, v122, v123
	v_add_f32_e32 v231, v120, v121
	v_mov_b32_e32 v232, v231
	v_cvt_pk_bf16_f32 v96, v96, v97
	v_cvt_pk_bf16_f32 v97, v98, v99
	s_waitcnt lgkmcnt(8)
	v_mfma_f32_32x32x16_bf16 v[144:159], v[244:247], v[174:177], v[144:159]
	v_cvt_pk_bf16_f32 v98, v100, v101
	v_cvt_pk_bf16_f32 v99, v102, v103
	v_cvt_pk_bf16_f32 v120, v104, v105
	v_cvt_pk_bf16_f32 v121, v106, v107
	v_cvt_pk_bf16_f32 v122, v108, v109
	v_cvt_pk_bf16_f32 v123, v110, v111
	v_cvt_pk_bf16_f32 v104, v112, v113
	v_cvt_pk_bf16_f32 v105, v114, v115
	v_cvt_pk_bf16_f32 v106, v116, v117
	v_cvt_pk_bf16_f32 v107, v118, v119
	v_cvt_pk_bf16_f32 v100, v190, v191
	v_cvt_pk_bf16_f32 v101, v192, v193
	v_cvt_pk_bf16_f32 v102, v124, v125
	v_cvt_pk_bf16_f32 v103, v126, v127
	s_nop 0
	v_permlane32_swap_b32_e32 v231, v232
	v_permlane32_swap_b32_e32 v96, v98
	v_permlane32_swap_b32_e32 v97, v99
	v_permlane32_swap_b32_e32 v120, v122
	v_permlane32_swap_b32_e32 v121, v123
	v_permlane32_swap_b32_e32 v104, v106
	v_permlane32_swap_b32_e32 v105, v107
	v_permlane32_swap_b32_e32 v100, v102
	v_permlane32_swap_b32_e32 v101, v103
	ds_read_b64_tr_b16 v[236:237], v234 offset:0x200
	ds_read_b64_tr_b16 v[238:239], v234 offset:0xa00
	ds_read_b64_tr_b16 v[240:241], v234 offset:0x1200
	ds_read_b64_tr_b16 v[242:243], v234 offset:0x1a00
	ds_read_b64_tr_b16 v[244:245], v234 offset:0x2200
	ds_read_b64_tr_b16 v[246:247], v234 offset:0x2a00
	ds_read_b64_tr_b16 v[190:191], v234 offset:0x3200
	ds_read_b64_tr_b16 v[192:193], v234 offset:0x3a00
	s_waitcnt lgkmcnt(8)
	s_nop 0
	v_mfma_f32_32x32x16_bf16 v[0:15], v[96:99], v[64:67], v[0:15]
	v_max_f32_e32 v108, v128, v129
	v_max3_f32 v109, v130, v131, v145
	v_max3_f32 v108, v108, v144, v146
	v_max3_f32 v108, v108, v147, v132
	v_max3_f32 v109, v109, v134, v135
	v_mfma_f32_32x32x16_bf16 v[0:15], v[120:123], v[68:71], v[0:15]
	v_max3_f32 v208, v108, v133, v148
	v_max3_f32 v209, v109, v150, v151
	v_mfma_f32_32x32x16_bf16 v[0:15], v[104:107], v[72:75], v[0:15]
	v_mfma_f32_32x32x16_bf16 v[0:15], v[100:103], v[76:79], v[0:15]
	ds_read_b64_tr_b16 v[124:125], v234 offset:0x400
	ds_read_b64_tr_b16 v[126:127], v234 offset:0xc00
	ds_read_b64_tr_b16 v[116:117], v234 offset:0x1400
	ds_read_b64_tr_b16 v[118:119], v234 offset:0x1c00
	ds_read_b64_tr_b16 v[112:113], v234 offset:0x2400
	ds_read_b64_tr_b16 v[114:115], v234 offset:0x2c00
	ds_read_b64_tr_b16 v[108:109], v234 offset:0x3400
	ds_read_b64_tr_b16 v[110:111], v234 offset:0x3c00
	s_waitcnt lgkmcnt(8)
	v_mfma_f32_32x32x16_bf16 v[48:63], v[96:99], v[236:239], v[48:63]
	v_max3_f32 v208, v208, v149, v136
	v_max3_f32 v209, v209, v138, v139
	v_max3_f32 v208, v208, v137, v152
	v_max3_f32 v209, v209, v154, v155
	v_max3_f32 v208, v208, v153, v140
	v_max3_f32 v209, v209, v142, v143
	v_max3_f32 v208, v208, v141, v156
	v_mfma_f32_32x32x16_bf16 v[48:63], v[120:123], v[240:243], v[48:63]
	v_max3_f32 v209, v209, v158, v159
	v_max3_f32 v208, v208, v157, v209
	v_mov_b32_e32 v209, v208
	s_nop 1
	v_permlane32_swap_b32_e32 v208, v209
	v_mfma_f32_32x32x16_bf16 v[48:63], v[104:107], v[244:247], v[48:63]
	v_max_f32_e32 v233, v208, v209
	v_mfma_f32_32x32x16_bf16 v[48:63], v[100:103], v[190:193], v[48:63]
	s_mov_b32 s2, 0x4138aa3b
	v_cmp_ge_f32_e32 vcc, s2, v233
	s_cmp_eq_u64 vcc, exec
	s_cbranch_scc0 .LBB0_836
	v_mov_b32_e32 v233, 1.0

; __device__ __forceinline__ void qkt64c(f32x16& p0, f32x16& p1, const char* Ks, const bf16x8* qr, const f32x16& cinit, int r32, int hi) {
; #pragma unroll
;     for (int d0 = 0; d0 < 4; ++d0) { const int cb = (d0 * 16 + hi * 8) * 2;
;         const bf16x8 b0 = *reinterpret_cast<const bf16x8*>(Ks + kswz<64>(r32, cb));
;         const bf16x8 b1 = *reinterpret_cast<const bf16x8*>(Ks + kswz<64>(32 + r32, cb));
;         if (d0 == 0) { p0 = __builtin_amdgcn_mfma_f32_32x32x16_bf16(b0, qr[0], cinit, 0, 0, 0); p1 = __builtin_amdgcn_mfma_f32_32x32x16_bf16(b1, qr[0], cinit, 0, 0, 0); }
;         else { p0 = __builtin_amdgcn_mfma_f32_32x32x16_bf16(b0, qr[d0], p0, 0, 0, 0); p1 = __builtin_amdgcn_mfma_f32_32x32x16_bf16(b1, qr[d0], p1, 0, 0, 0); } }
; }
.LBB0_829:
	v_add_co_u32_e32 v96, vcc, 0x8a60000, v202
	s_waitcnt lgkmcnt(0)
	s_nop 0
	v_addc_co_u32_e32 v97, vcc, 0, v203, vcc
	v_add_co_u32_e32 v98, vcc, 0x8a70000, v202
	s_nop 1
	v_addc_co_u32_e32 v99, vcc, 0, v203, vcc
	v_add_co_u32_e32 v100, vcc, 0x6a60000, v204
	s_nop 1
	v_addc_co_u32_e32 v101, vcc, 0, v205, vcc
	s_barrier
	v_add_u32_e32 v102, s2, v223
	ds_read_b128 v[112:115], v102 offset:49152
	v_add_u32_e32 v103, s2, v226
	ds_read_b128 v[116:119], v103 offset:49152
	v_add_u32_e32 v104, s2, v228
	ds_read_b128 v[120:123], v104 offset:49152
	v_add_u32_e32 v105, s2, v229
	ds_read_b128 v[124:127], v105 offset:49152
	ds_read_b128 v[190:193], v102 offset:53248
	ds_read_b128 v[202:205], v103 offset:53248
	ds_read_b128 v[234:237], v104 offset:53248
	ds_read_b128 v[238:241], v105 offset:53248
	global_load_dwordx4 v[178:181], v[96:97], off
	global_load_dwordx4 v[182:185], v[98:99], off
	global_load_dwordx4 v[186:189], v[100:101], off
	v_exp_f32_e32 v208, v152
	v_exp_f32_e32 v209, v153
	v_add_f32_e32 v152, v128, v129
	v_add_f32_e32 v153, v130, v131
	s_waitcnt lgkmcnt(7)
	v_mfma_f32_32x32x16_bf16 v[96:111], v[112:115], v[162:165], v[80:95]
	v_exp_f32_e32 v210, v154
	v_add_f32_e32 v152, v152, v153
	v_add_f32_e32 v153, v132, v133
	v_add_f32_e32 v154, v134, v135
	v_exp_f32_e32 v211, v155
	s_waitcnt lgkmcnt(6)
	v_mfma_f32_32x32x16_bf16 v[96:111], v[116:119], v[166:169], v[96:111]
	v_add_f32_e32 v153, v153, v154
	v_add_f32_e32 v154, v136, v137
	v_add_f32_e32 v155, v138, v139
	v_add_f32_e32 v154, v154, v155
	v_add_f32_e32 v155, v140, v141
	s_waitcnt lgkmcnt(5)
	v_mfma_f32_32x32x16_bf16 v[96:111], v[120:123], v[170:173], v[96:111]
	v_exp_f32_e32 v156, v156
	v_exp_f32_e32 v157, v157
	v_exp_f32_e32 v158, v158
	v_exp_f32_e32 v159, v159
	s_waitcnt lgkmcnt(4)
	v_mfma_f32_32x32x16_bf16 v[96:111], v[124:127], v[174:177], v[96:111]
	s_waitcnt lgkmcnt(3)
	v_mfma_f32_32x32x16_bf16 v[112:127], v[190:193], v[162:165], v[80:95]
	v_add_f32_e32 v190, v142, v143
	v_add_f32_e32 v155, v155, v190
	v_add_f32_e32 v190, v144, v145
	v_add_f32_e32 v191, v146, v147
	v_add_f32_e32 v190, v190, v191
	v_add_f32_e32 v152, v152, v190
	v_add_f32_e32 v190, v148, v149
	s_waitcnt lgkmcnt(2)
	v_mfma_f32_32x32x16_bf16 v[112:127], v[202:205], v[166:169], v[112:127]
	v_lshl_add_u32 v205, s42, 14, v217
	ds_read_b64_tr_b16 v[64:65], v205 offset:0
	ds_read_b64_tr_b16 v[66:67], v205 offset:0x800
	ds_read_b64_tr_b16 v[68:69], v205 offset:0x1000
	ds_read_b64_tr_b16 v[70:71], v205 offset:0x1800
	ds_read_b64_tr_b16 v[72:73], v205 offset:0x2000
	ds_read_b64_tr_b16 v[74:75], v205 offset:0x2800
	ds_read_b64_tr_b16 v[76:77], v205 offset:0x3000
	ds_read_b64_tr_b16 v[78:79], v205 offset:0x3800
	v_add_f32_e32 v191, v150, v151
	v_add_f32_e32 v190, v190, v191
	v_add_f32_e32 v153, v153, v190
	v_add_f32_e32 v190, v208, v209
	v_add_f32_e32 v191, v210, v211
	v_add_f32_e32 v190, v190, v191
	v_add_f32_e32 v154, v154, v190
	s_waitcnt lgkmcnt(9)
	v_mfma_f32_32x32x16_bf16 v[112:127], v[234:237], v[170:173], v[112:127]
	v_add_f32_e32 v190, v156, v157
	v_add_f32_e32 v191, v158, v159
	v_add_f32_e32 v190, v190, v191
	v_add_f32_e32 v155, v155, v190
	v_add_f32_e32 v152, v152, v153
	v_add_f32_e32 v153, v154, v155
	v_add_f32_e32 v203, v152, v153
	s_waitcnt lgkmcnt(8)
	v_mfma_f32_32x32x16_bf16 v[112:127], v[238:241], v[174:177], v[112:127]
	v_mov_b32_e32 v204, v203
	v_cvt_pk_bf16_f32 v152, v128, v129
	v_cvt_pk_bf16_f32 v153, v130, v131
	v_cvt_pk_bf16_f32 v154, v132, v133
	v_cvt_pk_bf16_f32 v155, v134, v135
	v_cvt_pk_bf16_f32 v136, v136, v137
	v_cvt_pk_bf16_f32 v137, v138, v139
	v_cvt_pk_bf16_f32 v138, v140, v141
	v_cvt_pk_bf16_f32 v139, v142, v143
	v_cvt_pk_bf16_f32 v132, v144, v145
	v_cvt_pk_bf16_f32 v133, v146, v147
	v_cvt_pk_bf16_f32 v134, v148, v149
	v_cvt_pk_bf16_f32 v135, v150, v151
	v_cvt_pk_bf16_f32 v128, v208, v209
	v_cvt_pk_bf16_f32 v129, v210, v211
	v_cvt_pk_bf16_f32 v130, v156, v157
	v_cvt_pk_bf16_f32 v131, v158, v159
	s_nop 1
	v_permlane32_swap_b32_e32 v203, v204
	v_permlane32_swap_b32_e32 v152, v154
	v_permlane32_swap_b32_e32 v153, v155
	v_permlane32_swap_b32_e32 v136, v138
	v_permlane32_swap_b32_e32 v137, v139
	v_permlane32_swap_b32_e32 v132, v134
	v_permlane32_swap_b32_e32 v133, v135
	v_permlane32_swap_b32_e32 v128, v130
	v_permlane32_swap_b32_e32 v129, v131
	ds_read_b64_tr_b16 v[190:191], v205 offset:0x200
	ds_read_b64_tr_b16 v[192:193], v205 offset:0xa00
	ds_read_b64_tr_b16 v[234:235], v205 offset:0x1200
	ds_read_b64_tr_b16 v[236:237], v205 offset:0x1a00
	ds_read_b64_tr_b16 v[238:239], v205 offset:0x2200
	ds_read_b64_tr_b16 v[240:241], v205 offset:0x2a00
	ds_read_b64_tr_b16 v[242:243], v205 offset:0x3200
	ds_read_b64_tr_b16 v[244:245], v205 offset:0x3a00
	s_waitcnt lgkmcnt(8)
	s_nop 0
	v_mfma_f32_32x32x16_bf16 v[0:15], v[152:155], v[64:67], v[0:15]
	v_max_f32_e32 v140, v96, v97
	v_max3_f32 v140, v140, v112, v114
	v_max3_f32 v141, v98, v99, v113
	v_max3_f32 v140, v140, v115, v100
	v_max3_f32 v141, v141, v102, v103
	v_mfma_f32_32x32x16_bf16 v[0:15], v[136:139], v[68:71], v[0:15]
	v_max3_f32 v202, v140, v101, v116
	v_max3_f32 v208, v141, v118, v119
	v_mfma_f32_32x32x16_bf16 v[0:15], v[132:135], v[72:75], v[0:15]
	v_mfma_f32_32x32x16_bf16 v[0:15], v[128:131], v[76:79], v[0:15]
	ds_read_b64_tr_b16 v[156:157], v205 offset:0x400
	ds_read_b64_tr_b16 v[158:159], v205 offset:0xc00
	ds_read_b64_tr_b16 v[148:149], v205 offset:0x1400
	ds_read_b64_tr_b16 v[150:151], v205 offset:0x1c00
	ds_read_b64_tr_b16 v[144:145], v205 offset:0x2400
	ds_read_b64_tr_b16 v[146:147], v205 offset:0x2c00
	ds_read_b64_tr_b16 v[140:141], v205 offset:0x3400
	ds_read_b64_tr_b16 v[142:143], v205 offset:0x3c00
	s_waitcnt lgkmcnt(8)
	v_mfma_f32_32x32x16_bf16 v[48:63], v[152:155], v[190:193], v[48:63]
	v_max3_f32 v190, v202, v117, v104
	v_max3_f32 v191, v208, v106, v107
	v_max3_f32 v190, v190, v105, v120
	v_max3_f32 v191, v191, v122, v123
	v_max3_f32 v190, v190, v121, v108
	v_max3_f32 v191, v191, v110, v111
	v_max3_f32 v190, v190, v109, v124
	v_mfma_f32_32x32x16_bf16 v[48:63], v[136:139], v[234:237], v[48:63]
	v_max3_f32 v191, v191, v126, v127
	v_max3_f32 v190, v190, v125, v191
	v_mov_b32_e32 v191, v190
	s_nop 1
	v_permlane32_swap_b32_e32 v190, v191
	v_mfma_f32_32x32x16_bf16 v[48:63], v[132:135], v[238:241], v[48:63]
	v_max_f32_e32 v234, v190, v191
	v_mfma_f32_32x32x16_bf16 v[48:63], v[128:131], v[242:245], v[48:63]
	s_mov_b32 s2, 0x4138aa3b
	v_cmp_ge_f32_e32 vcc, s2, v234
	s_cmp_eq_u64 vcc, exec
	v_mov_b32_e32 v202, 1.0
	s_cbranch_scc0 .LBB0_837

; __device__ __forceinline__ void qkt64c(f32x16& p0, f32x16& p1, const char* Ks, const bf16x8* qr, const f32x16& cinit, int r32, int hi) {
; #pragma unroll
;     for (int d0 = 0; d0 < 4; ++d0) { const int cb = (d0 * 16 + hi * 8) * 2;
;         const bf16x8 b0 = *reinterpret_cast<const bf16x8*>(Ks + kswz<64>(r32, cb));
;         const bf16x8 b1 = *reinterpret_cast<const bf16x8*>(Ks + kswz<64>(32 + r32, cb));
;         if (d0 == 0) { p0 = __builtin_amdgcn_mfma_f32_32x32x16_bf16(b0, qr[0], cinit, 0, 0, 0); p1 = __builtin_amdgcn_mfma_f32_32x32x16_bf16(b1, qr[0], cinit, 0, 0, 0); }
;         else { p0 = __builtin_amdgcn_mfma_f32_32x32x16_bf16(b0, qr[d0], p0, 0, 0, 0); p1 = __builtin_amdgcn_mfma_f32_32x32x16_bf16(b1, qr[d0], p1, 0, 0, 0); } }
; }
.LBB0_846:
	s_lshl_b32 s2, s30, 13
	s_add_i32 s2, s2, 0
	v_add_u32_e32 v128, s2, v227
	ds_read_b128 v[144:147], v128 offset:49152
	v_add_u32_e32 v129, s2, v231
	ds_read_b128 v[148:151], v129 offset:49152
	v_add_u32_e32 v130, s2, v232
	ds_read_b128 v[152:155], v130 offset:49152
	v_add_u32_e32 v131, s2, v233
	ds_read_b128 v[156:159], v131 offset:49152
	ds_read_b128 v[190:193], v128 offset:53248
	ds_read_b128 v[236:239], v129 offset:53248
	ds_read_b128 v[240:243], v130 offset:53248
	ds_read_b128 v[244:247], v131 offset:53248
	v_lshl_add_u64 v[202:203], v[200:201], 0, s[64:65]
	s_mov_b32 s2, 0x8a40000
	v_add_co_u32_e32 v64, vcc, s2, v202
	s_mov_b32 s2, 0x8a50000
	s_nop 0
	v_addc_co_u32_e32 v65, vcc, 0, v203, vcc
	v_add_co_u32_e32 v66, vcc, s2, v202
	v_lshl_add_u64 v[204:205], v[198:199], 0, s[64:65]
	s_nop 0
	v_addc_co_u32_e32 v67, vcc, 0, v203, vcc
	s_mov_b32 s2, 0x6a40000
	global_load_dwordx4 v[178:181], v[64:65], off
	global_load_dwordx4 v[182:185], v[66:67], off
	v_add_co_u32_e32 v64, vcc, s2, v204
	s_nop 1
	v_addc_co_u32_e32 v65, vcc, 0, v205, vcc
	global_load_dwordx4 v[186:189], v[64:65], off offset:128
	v_exp_f32_e32 v208, v120
	v_exp_f32_e32 v209, v121
	v_add_f32_e32 v120, v96, v97
	v_add_f32_e32 v121, v98, v99
	s_waitcnt lgkmcnt(7)
	v_mfma_f32_32x32x16_bf16 v[128:143], v[144:147], v[162:165], v[80:95]
	v_exp_f32_e32 v210, v122
	v_add_f32_e32 v120, v120, v121
	v_add_f32_e32 v121, v100, v101
	v_add_f32_e32 v122, v102, v103
	v_exp_f32_e32 v211, v123
	s_waitcnt lgkmcnt(6)
	v_mfma_f32_32x32x16_bf16 v[128:143], v[148:151], v[166:169], v[128:143]
	v_add_f32_e32 v121, v121, v122
	v_add_f32_e32 v122, v104, v105
	v_add_f32_e32 v123, v106, v107
	v_add_f32_e32 v122, v122, v123
	v_add_f32_e32 v123, v108, v109
	s_waitcnt lgkmcnt(5)
	v_mfma_f32_32x32x16_bf16 v[128:143], v[152:155], v[170:173], v[128:143]
	v_exp_f32_e32 v124, v124
	v_exp_f32_e32 v125, v125
	v_exp_f32_e32 v126, v126
	v_exp_f32_e32 v127, v127
	v_cvt_pk_bf16_f32 v96, v96, v97
	s_waitcnt lgkmcnt(4)
	v_mfma_f32_32x32x16_bf16 v[128:143], v[156:159], v[174:177], v[128:143]
	v_cvt_pk_bf16_f32 v97, v98, v99
	v_cvt_pk_bf16_f32 v98, v100, v101
	v_cvt_pk_bf16_f32 v99, v102, v103
	s_nop 0
	v_permlane32_swap_b32_e32 v96, v98
	s_waitcnt lgkmcnt(3)
	v_mfma_f32_32x32x16_bf16 v[144:159], v[190:193], v[162:165], v[80:95]
	v_add_f32_e32 v190, v110, v111
	v_add_f32_e32 v123, v123, v190
	v_add_f32_e32 v190, v112, v113
	v_add_f32_e32 v191, v114, v115
	v_add_f32_e32 v190, v190, v191
	v_add_f32_e32 v120, v190, v120
	v_add_f32_e32 v190, v116, v117
	s_waitcnt lgkmcnt(2)
	v_mfma_f32_32x32x16_bf16 v[144:159], v[236:239], v[166:169], v[144:159]
	v_lshl_add_u32 v238, s12, 14, v221
	ds_read_b64_tr_b16 v[64:65], v238 offset:0
	ds_read_b64_tr_b16 v[66:67], v238 offset:0x800
	ds_read_b64_tr_b16 v[68:69], v238 offset:0x1000
	ds_read_b64_tr_b16 v[70:71], v238 offset:0x1800
	ds_read_b64_tr_b16 v[72:73], v238 offset:0x2000
	ds_read_b64_tr_b16 v[74:75], v238 offset:0x2800
	ds_read_b64_tr_b16 v[76:77], v238 offset:0x3000
	ds_read_b64_tr_b16 v[78:79], v238 offset:0x3800
	v_add_f32_e32 v191, v118, v119
	v_add_f32_e32 v190, v190, v191
	v_add_f32_e32 v121, v190, v121
	v_add_f32_e32 v190, v208, v209
	v_add_f32_e32 v191, v210, v211
	v_add_f32_e32 v190, v190, v191
	v_add_f32_e32 v122, v122, v190
	s_waitcnt lgkmcnt(9)
	v_mfma_f32_32x32x16_bf16 v[144:159], v[240:243], v[170:173], v[144:159]
	v_add_f32_e32 v190, v124, v125
	v_add_f32_e32 v191, v126, v127
	v_add_f32_e32 v190, v190, v191
	v_add_f32_e32 v123, v123, v190
	v_add_f32_e32 v120, v120, v121
	v_add_f32_e32 v121, v122, v123
	v_add_f32_e32 v235, v120, v121
	s_waitcnt lgkmcnt(8)
	v_mfma_f32_32x32x16_bf16 v[144:159], v[244:247], v[174:177], v[144:159]
	v_mov_b32_e32 v236, v235
	v_cvt_pk_bf16_f32 v120, v104, v105
	v_cvt_pk_bf16_f32 v121, v106, v107
	v_cvt_pk_bf16_f32 v122, v108, v109
	v_cvt_pk_bf16_f32 v123, v110, v111
	v_cvt_pk_bf16_f32 v104, v112, v113
	v_cvt_pk_bf16_f32 v105, v114, v115
	v_cvt_pk_bf16_f32 v106, v116, v117
	v_cvt_pk_bf16_f32 v107, v118, v119
	v_cvt_pk_bf16_f32 v100, v208, v209
	v_cvt_pk_bf16_f32 v101, v210, v211
	v_cvt_pk_bf16_f32 v102, v124, v125
	v_cvt_pk_bf16_f32 v103, v126, v127
	s_nop 1
	v_permlane32_swap_b32_e32 v235, v236
	v_permlane32_swap_b32_e32 v97, v99
	v_permlane32_swap_b32_e32 v120, v122
	v_permlane32_swap_b32_e32 v121, v123
	v_permlane32_swap_b32_e32 v104, v106
	v_permlane32_swap_b32_e32 v105, v107
	v_permlane32_swap_b32_e32 v100, v102
	v_permlane32_swap_b32_e32 v101, v103
	ds_read_b64_tr_b16 v[190:191], v238 offset:0x200
	ds_read_b64_tr_b16 v[192:193], v238 offset:0xa00
	ds_read_b64_tr_b16 v[240:241], v238 offset:0x1200
	ds_read_b64_tr_b16 v[242:243], v238 offset:0x1a00
	ds_read_b64_tr_b16 v[244:245], v238 offset:0x2200
	ds_read_b64_tr_b16 v[246:247], v238 offset:0x2a00
	ds_read_b64_tr_b16 v[208:209], v238 offset:0x3200
	ds_read_b64_tr_b16 v[210:211], v238 offset:0x3a00
	s_waitcnt lgkmcnt(8)
	s_nop 0
	v_mfma_f32_32x32x16_bf16 v[0:15], v[96:99], v[64:67], v[0:15]
	v_max_f32_e32 v108, v128, v129
	v_max3_f32 v108, v108, v144, v146
	v_max3_f32 v109, v130, v131, v145
	v_max3_f32 v108, v108, v147, v132
	v_max3_f32 v109, v109, v134, v135
	v_mfma_f32_32x32x16_bf16 v[0:15], v[120:123], v[68:71], v[0:15]
	v_max3_f32 v237, v108, v133, v148
	v_max3_f32 v239, v109, v150, v151
	v_mfma_f32_32x32x16_bf16 v[0:15], v[104:107], v[72:75], v[0:15]
	v_mfma_f32_32x32x16_bf16 v[0:15], v[100:103], v[76:79], v[0:15]
	ds_read_b64_tr_b16 v[124:125], v238 offset:0x400
	ds_read_b64_tr_b16 v[126:127], v238 offset:0xc00
	ds_read_b64_tr_b16 v[116:117], v238 offset:0x1400
	ds_read_b64_tr_b16 v[118:119], v238 offset:0x1c00
	ds_read_b64_tr_b16 v[112:113], v238 offset:0x2400
	ds_read_b64_tr_b16 v[114:115], v238 offset:0x2c00
	ds_read_b64_tr_b16 v[108:109], v238 offset:0x3400
	ds_read_b64_tr_b16 v[110:111], v238 offset:0x3c00
	s_waitcnt lgkmcnt(8)
	v_mfma_f32_32x32x16_bf16 v[48:63], v[96:99], v[190:193], v[48:63]
	v_max3_f32 v190, v237, v149, v136
	v_max3_f32 v191, v239, v138, v139
	v_max3_f32 v190, v190, v137, v152
	v_max3_f32 v191, v191, v154, v155
	v_max3_f32 v190, v190, v153, v140
	v_max3_f32 v191, v191, v142, v143
	v_max3_f32 v190, v190, v141, v156
	v_mfma_f32_32x32x16_bf16 v[48:63], v[120:123], v[240:243], v[48:63]
	v_max3_f32 v191, v191, v158, v159
	v_max3_f32 v190, v190, v157, v191
	v_mov_b32_e32 v191, v190
	s_nop 1
	v_permlane32_swap_b32_e32 v190, v191
	v_mfma_f32_32x32x16_bf16 v[48:63], v[104:107], v[244:247], v[48:63]
	v_max_f32_e32 v237, v190, v191
	v_mfma_f32_32x32x16_bf16 v[48:63], v[100:103], v[208:211], v[48:63]
	s_mov_b32 s2, 0x4138aa3b
	v_cmp_ge_f32_e32 vcc, s2, v237
	s_cmp_eq_u64 vcc, exec
	s_cbranch_scc0 .LBB0_859
	v_mov_b32_e32 v237, 1.0

; __device__ __forceinline__ void qkt64c(f32x16& p0, f32x16& p1, const char* Ks, const bf16x8* qr, const f32x16& cinit, int r32, int hi) {
; #pragma unroll
;     for (int d0 = 0; d0 < 4; ++d0) { const int cb = (d0 * 16 + hi * 8) * 2;
;         const bf16x8 b0 = *reinterpret_cast<const bf16x8*>(Ks + kswz<64>(r32, cb));
;         const bf16x8 b1 = *reinterpret_cast<const bf16x8*>(Ks + kswz<64>(32 + r32, cb));
;         if (d0 == 0) { p0 = __builtin_amdgcn_mfma_f32_32x32x16_bf16(b0, qr[0], cinit, 0, 0, 0); p1 = __builtin_amdgcn_mfma_f32_32x32x16_bf16(b1, qr[0], cinit, 0, 0, 0); }
;         else { p0 = __builtin_amdgcn_mfma_f32_32x32x16_bf16(b0, qr[d0], p0, 0, 0, 0); p1 = __builtin_amdgcn_mfma_f32_32x32x16_bf16(b1, qr[d0], p1, 0, 0, 0); } }
; }
.LBB0_852:
	v_add_co_u32_e32 v96, vcc, 0x8a60000, v202
	s_waitcnt lgkmcnt(0)
	s_nop 0
	v_addc_co_u32_e32 v97, vcc, 0, v203, vcc
	v_add_co_u32_e32 v98, vcc, 0x8a70000, v202
	s_nop 1
	v_addc_co_u32_e32 v99, vcc, 0, v203, vcc
	v_add_co_u32_e32 v100, vcc, 0x6a60000, v204
	s_nop 1
	v_addc_co_u32_e32 v101, vcc, 0, v205, vcc
	s_barrier
	v_add_u32_e32 v102, s2, v227
	ds_read_b128 v[112:115], v102 offset:49152
	v_add_u32_e32 v103, s2, v231
	ds_read_b128 v[116:119], v103 offset:49152
	v_add_u32_e32 v104, s2, v232
	ds_read_b128 v[120:123], v104 offset:49152
	v_add_u32_e32 v105, s2, v233
	ds_read_b128 v[124:127], v105 offset:49152
	ds_read_b128 v[190:193], v102 offset:53248
	ds_read_b128 v[202:205], v103 offset:53248
	ds_read_b128 v[208:211], v104 offset:53248
	ds_read_b128 v[238:241], v105 offset:53248
	global_load_dwordx4 v[178:181], v[96:97], off
	global_load_dwordx4 v[182:185], v[98:99], off
	global_load_dwordx4 v[186:189], v[100:101], off offset:128
	v_exp_f32_e32 v242, v152
	v_exp_f32_e32 v243, v153
	v_add_f32_e32 v152, v128, v129
	v_add_f32_e32 v153, v130, v131
	s_waitcnt lgkmcnt(7)
	v_mfma_f32_32x32x16_bf16 v[96:111], v[112:115], v[162:165], v[80:95]
	v_exp_f32_e32 v244, v154
	v_add_f32_e32 v152, v152, v153
	v_add_f32_e32 v153, v132, v133
	v_add_f32_e32 v154, v134, v135
	v_exp_f32_e32 v245, v155
	s_waitcnt lgkmcnt(6)
	v_mfma_f32_32x32x16_bf16 v[96:111], v[116:119], v[166:169], v[96:111]
	v_add_f32_e32 v153, v153, v154
	v_add_f32_e32 v154, v136, v137
	v_add_f32_e32 v155, v138, v139
	v_add_f32_e32 v154, v154, v155
	v_add_f32_e32 v155, v140, v141
	s_waitcnt lgkmcnt(5)
	v_mfma_f32_32x32x16_bf16 v[96:111], v[120:123], v[170:173], v[96:111]
	v_exp_f32_e32 v156, v156
	v_exp_f32_e32 v157, v157
	v_exp_f32_e32 v158, v158
	v_exp_f32_e32 v159, v159
	s_waitcnt lgkmcnt(4)
	v_mfma_f32_32x32x16_bf16 v[96:111], v[124:127], v[174:177], v[96:111]
	s_waitcnt lgkmcnt(3)
	v_mfma_f32_32x32x16_bf16 v[112:127], v[190:193], v[162:165], v[80:95]
	v_add_f32_e32 v190, v142, v143
	v_add_f32_e32 v155, v155, v190
	v_add_f32_e32 v190, v144, v145
	v_add_f32_e32 v191, v146, v147
	v_add_f32_e32 v190, v190, v191
	v_add_f32_e32 v152, v152, v190
	v_add_f32_e32 v190, v148, v149
	s_waitcnt lgkmcnt(2)
	v_mfma_f32_32x32x16_bf16 v[112:127], v[202:205], v[166:169], v[112:127]
	v_lshl_add_u32 v205, s30, 14, v221
	ds_read_b64_tr_b16 v[64:65], v205 offset:0
	ds_read_b64_tr_b16 v[66:67], v205 offset:0x800
	ds_read_b64_tr_b16 v[68:69], v205 offset:0x1000
	ds_read_b64_tr_b16 v[70:71], v205 offset:0x1800
	ds_read_b64_tr_b16 v[72:73], v205 offset:0x2000
	ds_read_b64_tr_b16 v[74:75], v205 offset:0x2800
	ds_read_b64_tr_b16 v[76:77], v205 offset:0x3000
	ds_read_b64_tr_b16 v[78:79], v205 offset:0x3800
	v_add_f32_e32 v191, v150, v151
	v_add_f32_e32 v190, v190, v191
	v_add_f32_e32 v153, v153, v190
	v_add_f32_e32 v190, v242, v243
	v_add_f32_e32 v191, v244, v245
	v_add_f32_e32 v190, v190, v191
	v_add_f32_e32 v154, v154, v190
	s_waitcnt lgkmcnt(9)
	v_mfma_f32_32x32x16_bf16 v[112:127], v[208:211], v[170:173], v[112:127]
	v_add_f32_e32 v190, v156, v157
	v_add_f32_e32 v191, v158, v159
	v_add_f32_e32 v190, v190, v191
	v_add_f32_e32 v155, v155, v190
	v_add_f32_e32 v152, v152, v153
	v_add_f32_e32 v153, v154, v155
	v_add_f32_e32 v203, v152, v153
	s_waitcnt lgkmcnt(8)
	v_mfma_f32_32x32x16_bf16 v[112:127], v[238:241], v[174:177], v[112:127]
	v_mov_b32_e32 v204, v203
	v_cvt_pk_bf16_f32 v152, v128, v129
	v_cvt_pk_bf16_f32 v153, v130, v131
	v_cvt_pk_bf16_f32 v154, v132, v133
	v_cvt_pk_bf16_f32 v155, v134, v135
	v_cvt_pk_bf16_f32 v136, v136, v137
	v_cvt_pk_bf16_f32 v137, v138, v139
	v_cvt_pk_bf16_f32 v138, v140, v141
	v_cvt_pk_bf16_f32 v139, v142, v143
	v_cvt_pk_bf16_f32 v132, v144, v145
	v_cvt_pk_bf16_f32 v133, v146, v147
	v_cvt_pk_bf16_f32 v134, v148, v149
	v_cvt_pk_bf16_f32 v135, v150, v151
	v_cvt_pk_bf16_f32 v128, v242, v243
	v_cvt_pk_bf16_f32 v129, v244, v245
	v_cvt_pk_bf16_f32 v130, v156, v157
	v_cvt_pk_bf16_f32 v131, v158, v159
	s_nop 1
	v_permlane32_swap_b32_e32 v203, v204
	v_permlane32_swap_b32_e32 v152, v154
	v_permlane32_swap_b32_e32 v153, v155
	v_permlane32_swap_b32_e32 v136, v138
	v_permlane32_swap_b32_e32 v137, v139
	v_permlane32_swap_b32_e32 v132, v134
	v_permlane32_swap_b32_e32 v133, v135
	v_permlane32_swap_b32_e32 v128, v130
	v_permlane32_swap_b32_e32 v129, v131
	ds_read_b64_tr_b16 v[190:191], v205 offset:0x200
	ds_read_b64_tr_b16 v[192:193], v205 offset:0xa00
	ds_read_b64_tr_b16 v[208:209], v205 offset:0x1200
	ds_read_b64_tr_b16 v[210:211], v205 offset:0x1a00
	ds_read_b64_tr_b16 v[238:239], v205 offset:0x2200
	ds_read_b64_tr_b16 v[240:241], v205 offset:0x2a00
	ds_read_b64_tr_b16 v[242:243], v205 offset:0x3200
	ds_read_b64_tr_b16 v[244:245], v205 offset:0x3a00
	s_waitcnt lgkmcnt(8)
	s_nop 0
	v_mfma_f32_32x32x16_bf16 v[0:15], v[152:155], v[64:67], v[0:15]
	v_max_f32_e32 v140, v96, v97
	v_max3_f32 v140, v140, v112, v114
	v_max3_f32 v141, v98, v99, v113
	v_max3_f32 v140, v140, v115, v100
	v_max3_f32 v141, v141, v102, v103
	v_mfma_f32_32x32x16_bf16 v[0:15], v[136:139], v[68:71], v[0:15]
	v_max3_f32 v202, v140, v101, v116
	v_max3_f32 v246, v141, v118, v119
	v_mfma_f32_32x32x16_bf16 v[0:15], v[132:135], v[72:75], v[0:15]
	v_mfma_f32_32x32x16_bf16 v[0:15], v[128:131], v[76:79], v[0:15]
	ds_read_b64_tr_b16 v[156:157], v205 offset:0x400
	ds_read_b64_tr_b16 v[158:159], v205 offset:0xc00
	ds_read_b64_tr_b16 v[148:149], v205 offset:0x1400
	ds_read_b64_tr_b16 v[150:151], v205 offset:0x1c00
	ds_read_b64_tr_b16 v[144:145], v205 offset:0x2400
	ds_read_b64_tr_b16 v[146:147], v205 offset:0x2c00
	ds_read_b64_tr_b16 v[140:141], v205 offset:0x3400
	ds_read_b64_tr_b16 v[142:143], v205 offset:0x3c00
	s_waitcnt lgkmcnt(8)
	v_mfma_f32_32x32x16_bf16 v[48:63], v[152:155], v[190:193], v[48:63]
	v_max3_f32 v190, v202, v117, v104
	v_max3_f32 v191, v246, v106, v107
	v_max3_f32 v190, v190, v105, v120
	v_max3_f32 v191, v191, v122, v123
	v_max3_f32 v190, v190, v121, v108
	v_max3_f32 v191, v191, v110, v111
	v_max3_f32 v190, v190, v109, v124
	v_mfma_f32_32x32x16_bf16 v[48:63], v[136:139], v[208:211], v[48:63]
	v_max3_f32 v191, v191, v126, v127
	v_max3_f32 v190, v190, v125, v191
	v_mov_b32_e32 v191, v190
	s_nop 1
	v_permlane32_swap_b32_e32 v190, v191
	v_mfma_f32_32x32x16_bf16 v[48:63], v[132:135], v[238:241], v[48:63]
	v_max_f32_e32 v238, v190, v191
	v_mfma_f32_32x32x16_bf16 v[48:63], v[128:131], v[242:245], v[48:63]
	s_mov_b32 s2, 0x4138aa3b
	v_cmp_ge_f32_e32 vcc, s2, v238
	s_cmp_eq_u64 vcc, exec
	v_mov_b32_e32 v202, 1.0
	s_cbranch_scc0 .LBB0_860
